# baseline (speedup 1.0000x reference)
.LBB10_5:
	s_or_b64 exec, exec, s[12:13]
	s_mul_i32 s7, s7, s30
	s_sub_i32 s12, s33, s7
	s_lshl_b32 s22, s12, 7
	s_ashr_i32 s23, s22, 31
	s_lshl_b64 s[28:29], s[22:23], 2
	s_waitcnt lgkmcnt(0)
	s_barrier
	v_lshl_add_u64 v[10:11], v[68:69], 0, s[28:29]
	global_load_dwordx4 v[6:9], v[10:11], off
	global_load_dwordx4 v[2:5], v[10:11], off offset:16
	v_lshl_add_u64 v[18:19], v[70:71], 0, s[28:29]
	global_load_dwordx4 v[14:17], v[18:19], off
	global_load_dwordx4 v[10:13], v[18:19], off offset:16
	v_and_b32_e32 v18, 64, v114
	v_add_u32_e32 v19, 0, v87
	v_add_u32_e32 v22, s5, v87
	v_add_u32_e32 v26, 0, v88
	v_add_u32_e32 v27, s5, v88
	v_add_u32_e32 v44, 64, v18
	ds_read_b128 v[18:21], v19
	ds_read_b128 v[22:25], v22
	ds_read_b128 v[34:37], v26
	ds_read_b128 v[38:41], v27
	s_waitcnt vmcnt(4)
	ds_read_b64 v[26:27], v89
	v_xor_b32_e32 v30, 8, v114
	v_or_b32_e32 v28, s6, v66
	v_xor_b32_e32 v31, 4, v114
	v_cmp_lt_i32_e64 s[2:3], v30, v44
	v_ashrrev_i32_e32 v29, 31, v28
	s_waitcnt lgkmcnt(3)
	v_pk_add_f32 v[20:21], v[20:21], v[24:25]
	v_cndmask_b32_e64 v30, v114, v30, s[2:3]
	v_cmp_lt_i32_e64 s[2:3], v31, v44
	v_pk_add_f32 v[18:19], v[18:19], v[22:23]
	s_waitcnt lgkmcnt(1)
	v_pk_add_f32 v[22:23], v[36:37], v[40:41]
	v_pk_add_f32 v[24:25], v[34:35], v[38:39]
	v_lshl_add_u64 v[42:43], v[28:29], 2, s[26:27]
	v_cndmask_b32_e64 v45, v114, v31, s[2:3]
	v_lshlrev_b32_e32 v33, 2, v30
	v_lshlrev_b32_e32 v34, 2, v45
	s_waitcnt vmcnt(3) lgkmcnt(0)
	v_pk_fma_f32 v[18:19], v[26:27], v[6:7], v[18:19] op_sel_hi:[0,1,1] neg_lo:[1,0,0] neg_hi:[1,0,0]
	s_waitcnt vmcnt(2)
	v_pk_fma_f32 v[24:25], v[26:27], v[2:3], v[24:25] op_sel_hi:[0,1,1] neg_lo:[1,0,0] neg_hi:[1,0,0]
	v_pk_fma_f32 v[20:21], v[26:27], v[8:9], v[20:21] op_sel_hi:[0,1,1] neg_lo:[1,0,0] neg_hi:[1,0,0]
	v_pk_fma_f32 v[30:31], v[26:27], v[4:5], v[22:23] op_sel_hi:[0,1,1] neg_lo:[1,0,0] neg_hi:[1,0,0]
	s_waitcnt vmcnt(1)
	v_pk_fma_f32 v[22:23], v[26:27], v[18:19], v[14:15] op_sel:[1,0,0]
	s_waitcnt vmcnt(0)
	v_pk_fma_f32 v[18:19], v[26:27], v[24:25], v[10:11] op_sel:[1,0,0]
	v_pk_fma_f32 v[24:25], v[26:27], v[20:21], v[16:17] op_sel:[1,0,0]
	v_pk_fma_f32 v[20:21], v[26:27], v[30:31], v[12:13] op_sel:[1,0,0]
	global_load_dword v31, v[42:43], off
	global_load_dword v39, v[42:43], off offset:128
	global_load_dword v38, v[42:43], off offset:256
	global_load_dword v32, v[42:43], off offset:384
	v_max_f32_e32 v30, v20, v21
	v_max_f32_e32 v26, v22, v23
	v_max_f32_e32 v27, v24, v25
	v_max3_f32 v30, v18, v19, v30
	v_max3_f32 v26, v26, v27, v30
	s_nop 1
	v_mov_b32_dpp v27, v26 row_mirror row_mask:0xf bank_mask:0xf
	v_xor_b32_e32 v30, 2, v114
	v_cmp_lt_i32_e64 s[2:3], v30, v44
	s_waitcnt lgkmcnt(0)
	v_max_f32_e32 v27, v27, v27
	v_max_f32_e32 v26, v26, v27
	s_nop 1
	v_mov_b32_dpp v27, v26 row_half_mirror row_mask:0xf bank_mask:0xf
	v_cndmask_b32_e64 v30, v114, v30, s[2:3]
	v_lshlrev_b32_e32 v35, 2, v30
	v_xor_b32_e32 v30, 1, v114
	v_cmp_lt_i32_e64 s[2:3], v30, v44
	s_waitcnt lgkmcnt(0)
	v_max_f32_e32 v27, v27, v27
	v_max_f32_e32 v26, v26, v27
	s_nop 1
	v_mov_b32_dpp v27, v26 quad_perm:[2,3,0,1] row_mask:0xf bank_mask:0xf
	v_cndmask_b32_e64 v30, v114, v30, s[2:3]
	v_lshlrev_b32_e32 v36, 2, v30
	s_waitcnt lgkmcnt(0)
	v_max_f32_e32 v27, v27, v27
	v_max_f32_e32 v26, v26, v27
	s_nop 1
	v_mov_b32_dpp v27, v26 quad_perm:[1,0,3,2] row_mask:0xf bank_mask:0xf
	s_waitcnt lgkmcnt(0)
	v_max_f32_e32 v27, v27, v27
	v_max_f32_e32 v30, v26, v27
	v_sub_f32_e32 v26, v22, v30
	v_sub_f32_e32 v27, v18, v30
	v_sub_f32_e32 v37, v23, v30
	v_sub_f32_e32 v40, v19, v30
	v_mul_f32_e32 v26, 0x3fb8aa3b, v26
	v_mul_f32_e32 v27, 0x3fb8aa3b, v27
	v_sub_f32_e32 v41, v24, v30
	v_sub_f32_e32 v42, v20, v30
	v_mul_f32_e32 v37, 0x3fb8aa3b, v37
	v_mul_f32_e32 v40, 0x3fb8aa3b, v40
	v_exp_f32_e32 v26, v26
	v_exp_f32_e32 v27, v27
	v_sub_f32_e32 v43, v25, v30
	v_sub_f32_e32 v44, v21, v30
	v_mul_f32_e32 v41, 0x3fb8aa3b, v41
	v_mul_f32_e32 v42, 0x3fb8aa3b, v42
	v_exp_f32_e32 v37, v37
	v_exp_f32_e32 v40, v40
	v_mul_f32_e32 v43, 0x3fb8aa3b, v43
	v_mul_f32_e32 v44, 0x3fb8aa3b, v44
	v_exp_f32_e32 v41, v41
	v_exp_f32_e32 v42, v42
	v_exp_f32_e32 v43, v43
	v_exp_f32_e32 v44, v44
	v_add_f32_e32 v26, v26, v27
	v_add_f32_e32 v27, v37, v40
	v_add_f32_e32 v26, 0, v26
	v_add_f32_e32 v37, v41, v42
	v_add_f32_e32 v26, v26, v27
	v_add_f32_e32 v26, v26, v37
	v_add_f32_e32 v27, v43, v44
	v_add_f32_e32 v26, v26, v27
	s_nop 1
	v_mov_b32_dpp v27, v26 row_mirror row_mask:0xf bank_mask:0xf
	s_waitcnt lgkmcnt(0)
	v_add_f32_e32 v37, v26, v27
	s_nop 1
	v_mov_b32_dpp v40, v37 row_half_mirror row_mask:0xf bank_mask:0xf
	v_lshl_add_u64 v[26:27], v[72:73], 0, s[28:29]
	s_waitcnt lgkmcnt(0)
	v_add_f32_e32 v44, v37, v40
	s_nop 1
	v_mov_b32_dpp v45, v44 quad_perm:[2,3,0,1] row_mask:0xf bank_mask:0xf
	v_mad_i64_i32 v[40:41], s[2:3], v28, s14, 0
	v_lshl_add_u64 v[42:43], v[40:41], 2, v[26:27]
	v_or_b32_e32 v37, s22, v80
	s_waitcnt lgkmcnt(0)
	v_add_f32_e32 v40, v44, v45
	s_nop 1
	v_mov_b32_dpp v41, v40 quad_perm:[1,0,3,2] row_mask:0xf bank_mask:0xf
	global_store_dwordx4 v[42:43], v[22:25], off sc1
	global_store_dwordx4 v[42:43], v[18:21], off offset:16 sc1
	s_waitcnt vmcnt(5)
	v_sub_u32_e32 v42, v31, v37
	v_cmp_gt_u32_e64 s[2:3], 8, v42
	s_and_saveexec_b64 s[22:23], s[2:3]
	s_cbranch_execz .LBB10_7
	v_cmp_eq_u32_e64 s[2:3], v31, v37
	s_nop 1
	v_cndmask_b32_e64 v22, 0, v22, s[2:3]
	v_cmp_eq_u32_e64 s[2:3], 4, v42
	s_nop 1
	v_cndmask_b32_e64 v18, v22, v18, s[2:3]
	v_cmp_eq_u32_e64 s[2:3], 1, v42
	s_nop 1
	v_cndmask_b32_e64 v18, v18, v23, s[2:3]
	v_cmp_eq_u32_e64 s[2:3], 5, v42
	s_nop 1
	v_cndmask_b32_e64 v18, v18, v19, s[2:3]
	v_cmp_eq_u32_e64 s[2:3], 2, v42
	s_nop 1
	v_cndmask_b32_e64 v18, v18, v24, s[2:3]
	v_cmp_eq_u32_e64 s[2:3], 6, v42
	s_nop 1
	v_cndmask_b32_e64 v18, v18, v20, s[2:3]
	v_cmp_eq_u32_e64 s[2:3], 3, v42
	s_nop 1
	v_cndmask_b32_e64 v18, v18, v25, s[2:3]
	v_cmp_eq_u32_e64 s[2:3], 7, v42
	s_nop 1
	v_cndmask_b32_e64 v20, v18, v21, s[2:3]
	v_lshl_add_u64 v[18:19], v[28:29], 2, s[24:25]
	global_store_dword v[18:19], v20, off

.LBB10_9:
	s_or_b64 exec, exec, s[2:3]
	v_add_u32_e32 v18, 0, v91
	v_add_u32_e32 v22, s5, v91
	v_add_u32_e32 v28, 0, v92
	v_add_u32_e32 v40, s5, v92
	ds_read_b128 v[18:21], v18
	ds_read_b128 v[22:25], v22
	ds_read_b128 v[28:31], v28
	ds_read_b64 v[44:45], v93
	s_waitcnt lgkmcnt(4)
	ds_read_b128 v[40:43], v40
	s_waitcnt lgkmcnt(3)
	v_pk_add_f32 v[20:21], v[20:21], v[24:25]
	v_pk_add_f32 v[18:19], v[18:19], v[22:23]
	s_waitcnt lgkmcnt(0)
	v_pk_add_f32 v[24:25], v[30:31], v[42:43]
	v_pk_add_f32 v[22:23], v[28:29], v[40:41]
	v_pk_fma_f32 v[24:25], v[44:45], v[4:5], v[24:25] op_sel_hi:[0,1,1] neg_lo:[1,0,0] neg_hi:[1,0,0]
	v_pk_fma_f32 v[18:19], v[44:45], v[6:7], v[18:19] op_sel_hi:[0,1,1] neg_lo:[1,0,0] neg_hi:[1,0,0]
	v_pk_fma_f32 v[22:23], v[44:45], v[2:3], v[22:23] op_sel_hi:[0,1,1] neg_lo:[1,0,0] neg_hi:[1,0,0]
	v_pk_fma_f32 v[20:21], v[44:45], v[8:9], v[20:21] op_sel_hi:[0,1,1] neg_lo:[1,0,0] neg_hi:[1,0,0]
	v_pk_fma_f32 v[24:25], v[44:45], v[24:25], v[12:13] op_sel:[1,0,0]
	v_pk_fma_f32 v[18:19], v[44:45], v[18:19], v[14:15] op_sel:[1,0,0]
	v_pk_fma_f32 v[22:23], v[44:45], v[22:23], v[10:11] op_sel:[1,0,0]
	v_pk_fma_f32 v[20:21], v[44:45], v[20:21], v[16:17] op_sel:[1,0,0]
	v_max_f32_e32 v30, v24, v25
	v_max_f32_e32 v28, v18, v19
	v_max_f32_e32 v29, v20, v21
	v_max3_f32 v30, v22, v23, v30
	v_max3_f32 v28, v28, v29, v30
	s_nop 1
	v_mov_b32_dpp v29, v28 row_mirror row_mask:0xf bank_mask:0xf
	s_waitcnt lgkmcnt(0)
	v_max_f32_e32 v29, v29, v29
	v_max_f32_e32 v28, v28, v29
	s_nop 1
	v_mov_b32_dpp v29, v28 row_half_mirror row_mask:0xf bank_mask:0xf
	s_waitcnt lgkmcnt(0)
	v_max_f32_e32 v29, v29, v29
	v_max_f32_e32 v28, v28, v29
	s_nop 1
	v_mov_b32_dpp v29, v28 quad_perm:[2,3,0,1] row_mask:0xf bank_mask:0xf
	s_waitcnt lgkmcnt(0)
	v_max_f32_e32 v29, v29, v29
	v_max_f32_e32 v28, v28, v29
	s_nop 1
	v_mov_b32_dpp v29, v28 quad_perm:[1,0,3,2] row_mask:0xf bank_mask:0xf
	s_waitcnt lgkmcnt(0)
	v_max_f32_e32 v29, v29, v29
	v_max_f32_e32 v28, v28, v29
	v_sub_f32_e32 v29, v18, v28
	v_sub_f32_e32 v30, v22, v28
	v_sub_f32_e32 v31, v19, v28
	v_sub_f32_e32 v40, v23, v28
	v_mul_f32_e32 v29, 0x3fb8aa3b, v29
	v_mul_f32_e32 v30, 0x3fb8aa3b, v30
	v_mul_f32_e32 v31, 0x3fb8aa3b, v31
	v_mul_f32_e32 v40, 0x3fb8aa3b, v40
	v_exp_f32_e32 v29, v29
	v_exp_f32_e32 v30, v30
	v_exp_f32_e32 v31, v31
	v_exp_f32_e32 v40, v40
	v_sub_f32_e32 v41, v21, v28
	v_add_f32_e32 v29, v29, v30
	v_sub_f32_e32 v42, v25, v28
	v_add_f32_e32 v30, v31, v40
	v_sub_f32_e32 v31, v20, v28
	v_sub_f32_e32 v40, v24, v28
	v_mul_f32_e32 v31, 0x3fb8aa3b, v31
	v_mul_f32_e32 v40, 0x3fb8aa3b, v40
	v_exp_f32_e32 v31, v31
	v_exp_f32_e32 v40, v40
	v_mul_f32_e32 v41, 0x3fb8aa3b, v41
	v_mul_f32_e32 v42, 0x3fb8aa3b, v42
	v_exp_f32_e32 v41, v41
	v_exp_f32_e32 v42, v42
	v_add_f32_e32 v29, 0, v29
	v_add_f32_e32 v29, v29, v30
	v_add_f32_e32 v30, v31, v40
	v_add_f32_e32 v29, v29, v30
	v_add_f32_e32 v30, v41, v42
	v_add_f32_e32 v29, v29, v30
	s_nop 1
	v_mov_b32_dpp v30, v29 row_mirror row_mask:0xf bank_mask:0xf
	s_waitcnt lgkmcnt(0)
	v_add_f32_e32 v29, v29, v30
	s_nop 1
	v_mov_b32_dpp v30, v29 row_half_mirror row_mask:0xf bank_mask:0xf
	s_waitcnt lgkmcnt(0)
	v_add_f32_e32 v29, v29, v30
	s_nop 1
	v_mov_b32_dpp v31, v29 quad_perm:[2,3,0,1] row_mask:0xf bank_mask:0xf
	v_or_b32_e32 v30, s6, v90
	v_mad_i64_i32 v[40:41], s[2:3], v30, s14, 0
	v_lshl_add_u64 v[42:43], v[40:41], 2, v[26:27]
	s_waitcnt lgkmcnt(0)
	v_add_f32_e32 v29, v29, v31
	s_nop 1
	v_mov_b32_dpp v40, v29 quad_perm:[1,0,3,2] row_mask:0xf bank_mask:0xf
	s_waitcnt vmcnt(4)
	v_sub_u32_e32 v31, v39, v37
	v_cmp_gt_u32_e64 s[2:3], 8, v31
	global_store_dwordx4 v[42:43], v[18:21], off sc1
	global_store_dwordx4 v[42:43], v[22:25], off offset:16 sc1
	s_and_saveexec_b64 s[22:23], s[2:3]
	s_cbranch_execz .LBB10_11
	v_cmp_eq_u32_e64 s[2:3], v39, v37
	s_ashr_i32 s7, s6, 31
	s_nop 0
	v_cndmask_b32_e64 v18, 0, v18, s[2:3]
	v_cmp_eq_u32_e64 s[2:3], 4, v31
	s_nop 1
	v_cndmask_b32_e64 v18, v18, v22, s[2:3]
	v_cmp_eq_u32_e64 s[2:3], 1, v31
	s_nop 1
	v_cndmask_b32_e64 v18, v18, v19, s[2:3]
	v_cmp_eq_u32_e64 s[2:3], 5, v31
	s_nop 1
	v_cndmask_b32_e64 v18, v18, v23, s[2:3]
	v_cmp_eq_u32_e64 s[2:3], 2, v31
	s_nop 1
	v_cndmask_b32_e64 v18, v18, v20, s[2:3]
	v_cmp_eq_u32_e64 s[2:3], 6, v31
	s_nop 1
	v_cndmask_b32_e64 v18, v18, v24, s[2:3]
	v_cmp_eq_u32_e64 s[2:3], 3, v31
	s_nop 1
	v_cndmask_b32_e64 v18, v18, v21, s[2:3]
	v_cmp_eq_u32_e64 s[2:3], 7, v31
	s_nop 1
	v_cndmask_b32_e64 v20, v18, v25, s[2:3]
	v_lshl_add_u64 v[18:19], v[66:67], 0, s[6:7]
	v_lshl_add_u64 v[18:19], v[18:19], 2, s[24:25]
	global_store_dword v[18:19], v20, off offset:128

.LBB10_13:
	s_or_b64 exec, exec, s[2:3]
	v_add_u32_e32 v18, 0, v95
	v_add_u32_e32 v22, s5, v95
	v_add_u32_e32 v28, 0, v96
	v_add_u32_e32 v39, s5, v96
	ds_read_b128 v[18:21], v18
	ds_read_b128 v[22:25], v22
	ds_read_b128 v[28:31], v28
	ds_read_b64 v[44:45], v97
	s_waitcnt lgkmcnt(4)
	ds_read_b128 v[40:43], v39
	s_waitcnt lgkmcnt(3)
	v_pk_add_f32 v[20:21], v[20:21], v[24:25]
	v_pk_add_f32 v[18:19], v[18:19], v[22:23]
	s_waitcnt lgkmcnt(0)
	v_pk_add_f32 v[24:25], v[30:31], v[42:43]
	v_pk_add_f32 v[22:23], v[28:29], v[40:41]
	v_pk_fma_f32 v[24:25], v[44:45], v[4:5], v[24:25] op_sel_hi:[0,1,1] neg_lo:[1,0,0] neg_hi:[1,0,0]
	v_pk_fma_f32 v[18:19], v[44:45], v[6:7], v[18:19] op_sel_hi:[0,1,1] neg_lo:[1,0,0] neg_hi:[1,0,0]
	v_pk_fma_f32 v[22:23], v[44:45], v[2:3], v[22:23] op_sel_hi:[0,1,1] neg_lo:[1,0,0] neg_hi:[1,0,0]
	v_pk_fma_f32 v[20:21], v[44:45], v[8:9], v[20:21] op_sel_hi:[0,1,1] neg_lo:[1,0,0] neg_hi:[1,0,0]
	v_pk_fma_f32 v[24:25], v[44:45], v[24:25], v[12:13] op_sel:[1,0,0]
	v_pk_fma_f32 v[18:19], v[44:45], v[18:19], v[14:15] op_sel:[1,0,0]
	v_pk_fma_f32 v[22:23], v[44:45], v[22:23], v[10:11] op_sel:[1,0,0]
	v_pk_fma_f32 v[20:21], v[44:45], v[20:21], v[16:17] op_sel:[1,0,0]
	v_max_f32_e32 v30, v24, v25
	v_max_f32_e32 v28, v18, v19
	v_max_f32_e32 v29, v20, v21
	v_max3_f32 v30, v22, v23, v30
	v_max3_f32 v28, v28, v29, v30
	s_nop 1
	v_mov_b32_dpp v29, v28 row_mirror row_mask:0xf bank_mask:0xf
	s_waitcnt lgkmcnt(0)
	v_max_f32_e32 v29, v29, v29
	v_max_f32_e32 v28, v28, v29
	s_nop 1
	v_mov_b32_dpp v29, v28 row_half_mirror row_mask:0xf bank_mask:0xf
	s_waitcnt lgkmcnt(0)
	v_max_f32_e32 v29, v29, v29
	v_max_f32_e32 v28, v28, v29
	s_nop 1
	v_mov_b32_dpp v29, v28 quad_perm:[2,3,0,1] row_mask:0xf bank_mask:0xf
	s_waitcnt lgkmcnt(0)
	v_max_f32_e32 v29, v29, v29
	v_max_f32_e32 v28, v28, v29
	s_nop 1
	v_mov_b32_dpp v29, v28 quad_perm:[1,0,3,2] row_mask:0xf bank_mask:0xf
	s_waitcnt lgkmcnt(0)
	v_max_f32_e32 v29, v29, v29
	v_max_f32_e32 v28, v28, v29
	v_sub_f32_e32 v29, v18, v28
	v_sub_f32_e32 v30, v22, v28
	v_sub_f32_e32 v31, v19, v28
	v_sub_f32_e32 v39, v23, v28
	v_mul_f32_e32 v29, 0x3fb8aa3b, v29
	v_mul_f32_e32 v30, 0x3fb8aa3b, v30
	v_mul_f32_e32 v31, 0x3fb8aa3b, v31
	v_mul_f32_e32 v39, 0x3fb8aa3b, v39
	v_exp_f32_e32 v29, v29
	v_exp_f32_e32 v30, v30
	v_exp_f32_e32 v31, v31
	v_exp_f32_e32 v39, v39
	v_sub_f32_e32 v40, v21, v28
	v_add_f32_e32 v29, v29, v30
	v_sub_f32_e32 v41, v25, v28
	v_add_f32_e32 v30, v31, v39
	v_sub_f32_e32 v31, v20, v28
	v_sub_f32_e32 v39, v24, v28
	v_mul_f32_e32 v31, 0x3fb8aa3b, v31
	v_mul_f32_e32 v39, 0x3fb8aa3b, v39
	v_exp_f32_e32 v31, v31
	v_exp_f32_e32 v39, v39
	v_mul_f32_e32 v40, 0x3fb8aa3b, v40
	v_mul_f32_e32 v41, 0x3fb8aa3b, v41
	v_exp_f32_e32 v40, v40
	v_exp_f32_e32 v41, v41
	v_add_f32_e32 v29, 0, v29
	v_add_f32_e32 v29, v29, v30
	v_add_f32_e32 v30, v31, v39
	v_add_f32_e32 v29, v29, v30
	v_add_f32_e32 v30, v40, v41
	v_add_f32_e32 v29, v29, v30
	s_nop 1
	v_mov_b32_dpp v30, v29 row_mirror row_mask:0xf bank_mask:0xf
	s_waitcnt lgkmcnt(0)
	v_add_f32_e32 v29, v29, v30
	s_nop 1
	v_mov_b32_dpp v30, v29 row_half_mirror row_mask:0xf bank_mask:0xf
	s_waitcnt lgkmcnt(0)
	v_add_f32_e32 v29, v29, v30
	s_nop 1
	v_mov_b32_dpp v31, v29 quad_perm:[2,3,0,1] row_mask:0xf bank_mask:0xf
	v_or_b32_e32 v30, s6, v94
	v_mad_i64_i32 v[40:41], s[2:3], v30, s14, 0
	v_lshl_add_u64 v[40:41], v[40:41], 2, v[26:27]
	s_waitcnt lgkmcnt(0)
	v_add_f32_e32 v29, v29, v31
	s_nop 1
	v_mov_b32_dpp v39, v29 quad_perm:[1,0,3,2] row_mask:0xf bank_mask:0xf
	s_waitcnt vmcnt(5)
	v_sub_u32_e32 v31, v38, v37
	v_cmp_gt_u32_e64 s[2:3], 8, v31
	global_store_dwordx4 v[40:41], v[18:21], off sc1
	global_store_dwordx4 v[40:41], v[22:25], off offset:16 sc1
	s_and_saveexec_b64 s[22:23], s[2:3]
	s_cbranch_execz .LBB10_15
	v_cmp_eq_u32_e64 s[2:3], v38, v37
	s_ashr_i32 s7, s6, 31
	s_nop 0
	v_cndmask_b32_e64 v18, 0, v18, s[2:3]
	v_cmp_eq_u32_e64 s[2:3], 4, v31
	s_nop 1
	v_cndmask_b32_e64 v18, v18, v22, s[2:3]
	v_cmp_eq_u32_e64 s[2:3], 1, v31
	s_nop 1
	v_cndmask_b32_e64 v18, v18, v19, s[2:3]
	v_cmp_eq_u32_e64 s[2:3], 5, v31
	s_nop 1
	v_cndmask_b32_e64 v18, v18, v23, s[2:3]
	v_cmp_eq_u32_e64 s[2:3], 2, v31
	s_nop 1
	v_cndmask_b32_e64 v18, v18, v20, s[2:3]
	v_cmp_eq_u32_e64 s[2:3], 6, v31
	s_nop 1
	v_cndmask_b32_e64 v18, v18, v24, s[2:3]
	v_cmp_eq_u32_e64 s[2:3], 3, v31
	s_nop 1
	v_cndmask_b32_e64 v18, v18, v21, s[2:3]
	v_cmp_eq_u32_e64 s[2:3], 7, v31
	s_nop 1
	v_cndmask_b32_e64 v20, v18, v25, s[2:3]
	v_lshl_add_u64 v[18:19], v[66:67], 0, s[6:7]
	v_lshl_add_u64 v[18:19], v[18:19], 2, s[24:25]
	global_store_dword v[18:19], v20, off offset:256

.LBB10_17:
	s_or_b64 exec, exec, s[2:3]
	v_add_u32_e32 v18, 0, v99
	ds_read_b128 v[18:21], v18
	v_add_u32_e32 v22, s5, v99
	v_add_u32_e32 v28, 0, v100
	ds_read_b128 v[22:25], v22
	ds_read_b128 v[28:31], v28
	ds_read_b64 v[42:43], v101
	v_add_u32_e32 v38, s5, v100
	s_waitcnt lgkmcnt(4)
	ds_read_b128 v[38:41], v38
	s_waitcnt lgkmcnt(3)
	v_pk_add_f32 v[18:19], v[18:19], v[22:23]
	v_pk_add_f32 v[20:21], v[20:21], v[24:25]
	s_waitcnt lgkmcnt(1)
	v_pk_fma_f32 v[6:7], v[42:43], v[6:7], v[18:19] op_sel_hi:[0,1,1] neg_lo:[1,0,0] neg_hi:[1,0,0]
	v_pk_fma_f32 v[6:7], v[42:43], v[6:7], v[14:15] op_sel:[1,0,0]
	s_waitcnt lgkmcnt(0)
	v_pk_add_f32 v[14:15], v[30:31], v[40:41]
	v_pk_add_f32 v[18:19], v[28:29], v[38:39]
	v_pk_fma_f32 v[4:5], v[42:43], v[4:5], v[14:15] op_sel_hi:[0,1,1] neg_lo:[1,0,0] neg_hi:[1,0,0]
	v_pk_fma_f32 v[2:3], v[42:43], v[2:3], v[18:19] op_sel_hi:[0,1,1] neg_lo:[1,0,0] neg_hi:[1,0,0]
	v_pk_fma_f32 v[8:9], v[42:43], v[8:9], v[20:21] op_sel_hi:[0,1,1] neg_lo:[1,0,0] neg_hi:[1,0,0]
	v_pk_fma_f32 v[4:5], v[42:43], v[4:5], v[12:13] op_sel:[1,0,0]
	v_pk_fma_f32 v[2:3], v[42:43], v[2:3], v[10:11] op_sel:[1,0,0]
	v_pk_fma_f32 v[8:9], v[42:43], v[8:9], v[16:17] op_sel:[1,0,0]
	v_max_f32_e32 v12, v4, v5
	v_max_f32_e32 v10, v6, v7
	v_max_f32_e32 v11, v8, v9
	v_max3_f32 v12, v2, v3, v12
	v_max3_f32 v10, v10, v11, v12
	s_nop 1
	v_mov_b32_dpp v11, v10 row_mirror row_mask:0xf bank_mask:0xf
	s_waitcnt lgkmcnt(0)
	v_max_f32_e32 v11, v11, v11
	v_max_f32_e32 v10, v10, v11
	s_nop 1
	v_mov_b32_dpp v11, v10 row_half_mirror row_mask:0xf bank_mask:0xf
	s_waitcnt lgkmcnt(0)
	v_max_f32_e32 v11, v11, v11
	v_max_f32_e32 v10, v10, v11
	s_nop 1
	v_mov_b32_dpp v11, v10 quad_perm:[2,3,0,1] row_mask:0xf bank_mask:0xf
	s_waitcnt lgkmcnt(0)
	v_max_f32_e32 v11, v11, v11
	v_max_f32_e32 v10, v10, v11
	s_nop 1
	v_mov_b32_dpp v11, v10 quad_perm:[1,0,3,2] row_mask:0xf bank_mask:0xf
	s_waitcnt lgkmcnt(0)
	v_max_f32_e32 v11, v11, v11
	v_max_f32_e32 v10, v10, v11
	v_sub_f32_e32 v11, v6, v10
	v_sub_f32_e32 v12, v2, v10
	v_sub_f32_e32 v13, v7, v10
	v_sub_f32_e32 v14, v3, v10
	v_mul_f32_e32 v11, 0x3fb8aa3b, v11
	v_mul_f32_e32 v12, 0x3fb8aa3b, v12
	v_mul_f32_e32 v13, 0x3fb8aa3b, v13
	v_mul_f32_e32 v14, 0x3fb8aa3b, v14
	v_exp_f32_e32 v11, v11
	v_exp_f32_e32 v12, v12
	v_exp_f32_e32 v13, v13
	v_exp_f32_e32 v14, v14
	v_sub_f32_e32 v15, v9, v10
	v_add_f32_e32 v11, v11, v12
	v_sub_f32_e32 v16, v5, v10
	v_add_f32_e32 v12, v13, v14
	v_sub_f32_e32 v13, v8, v10
	v_sub_f32_e32 v14, v4, v10
	v_mul_f32_e32 v13, 0x3fb8aa3b, v13
	v_mul_f32_e32 v14, 0x3fb8aa3b, v14
	v_exp_f32_e32 v13, v13
	v_exp_f32_e32 v14, v14
	v_mul_f32_e32 v15, 0x3fb8aa3b, v15
	v_mul_f32_e32 v16, 0x3fb8aa3b, v16
	v_exp_f32_e32 v15, v15
	v_exp_f32_e32 v16, v16
	v_add_f32_e32 v11, 0, v11
	v_add_f32_e32 v11, v11, v12
	v_add_f32_e32 v12, v13, v14
	v_add_f32_e32 v11, v11, v12
	v_add_f32_e32 v12, v15, v16
	v_add_f32_e32 v11, v11, v12
	s_nop 1
	v_mov_b32_dpp v12, v11 row_mirror row_mask:0xf bank_mask:0xf
	s_waitcnt lgkmcnt(0)
	v_add_f32_e32 v11, v11, v12
	s_nop 1
	v_mov_b32_dpp v12, v11 row_half_mirror row_mask:0xf bank_mask:0xf
	s_waitcnt lgkmcnt(0)
	v_add_f32_e32 v11, v11, v12
	s_nop 1
	v_mov_b32_dpp v13, v11 quad_perm:[2,3,0,1] row_mask:0xf bank_mask:0xf
	v_add_u32_e32 v12, s6, v98
	v_mad_i64_i32 v[14:15], s[2:3], v12, s14, 0
	v_lshl_add_u64 v[16:17], v[14:15], 2, v[26:27]
	s_waitcnt lgkmcnt(0)
	v_add_f32_e32 v11, v11, v13
	s_nop 1
	v_mov_b32_dpp v14, v11 quad_perm:[1,0,3,2] row_mask:0xf bank_mask:0xf
	s_waitcnt vmcnt(6)
	v_sub_u32_e32 v13, v32, v37
	v_cmp_gt_u32_e64 s[2:3], 8, v13
	global_store_dwordx4 v[16:17], v[6:9], off sc1
	global_store_dwordx4 v[16:17], v[2:5], off offset:16 sc1
	s_and_saveexec_b64 s[22:23], s[2:3]
	s_cbranch_execz .LBB10_19
	v_cmp_eq_u32_e64 s[2:3], v32, v37
	s_ashr_i32 s7, s6, 31
	s_nop 0
	v_cndmask_b32_e64 v6, 0, v6, s[2:3]
	v_cmp_eq_u32_e64 s[2:3], 4, v13
	s_nop 1
	v_cndmask_b32_e64 v2, v6, v2, s[2:3]
	v_cmp_eq_u32_e64 s[2:3], 1, v13
	s_nop 1
	v_cndmask_b32_e64 v2, v2, v7, s[2:3]
	v_cmp_eq_u32_e64 s[2:3], 5, v13
	s_nop 1
	v_cndmask_b32_e64 v2, v2, v3, s[2:3]
	v_cmp_eq_u32_e64 s[2:3], 2, v13
	s_nop 1
	v_cndmask_b32_e64 v2, v2, v8, s[2:3]
	v_cmp_eq_u32_e64 s[2:3], 6, v13
	s_nop 1
	v_cndmask_b32_e64 v2, v2, v4, s[2:3]
	v_cmp_eq_u32_e64 s[2:3], 3, v13
	s_nop 1
	v_cndmask_b32_e64 v2, v2, v9, s[2:3]
	v_cmp_eq_u32_e64 s[2:3], 7, v13
	s_nop 1
	v_cndmask_b32_e64 v4, v2, v5, s[2:3]
	v_lshl_add_u64 v[2:3], v[66:67], 0, s[6:7]
	v_lshl_add_u64 v[2:3], v[2:3], 2, s[24:25]
	global_store_dword v[2:3], v4, off offset:384
